# P8 epilogue: residual loads of 6 row groups in flight, counted vmcnt, PSQ stores batched
# baseline (speedup 1.0000x reference)
; __device__ __forceinline__ int fresh_lane() { int l; asm volatile("v_mbcnt_lo_u32_b32 %0, -1, 0\n\tv_mbcnt_hi_u32_b32 %0, -1, %0" : "=v"(l)); return l; }
; __device__ __forceinline__ unsigned cvt_pk_bf16(float lo, float hi) { unsigned r; asm volatile("v_cvt_pk_bf16_f32 %0, %1, %2" : "=v"(r) : "v"(lo), "v"(hi)); return r; }
;     __device__ __forceinline__ void operator()(const f32x4 (&acc)[2][2][4][2], const Unit& u, int wr, int wc, int fr_, int fq_) const {
;         const int l_ = fresh_lane(), fr = l_ & 15, fq = l_ >> 4;
;         const int row0 = u.pm * BM + wr * 64 + fr, col0 = u.pn * BM + wc * 32 + 4 * fq;
; #pragma unroll
;         for (int ai = 0; ai < 2; ++ai)
; #pragma unroll
;             for (int m = 0; m < 4; ++m) { const size_t r = (size_t)(row0 + ai * HALF + m * 16); float ss = 0.f;
; #pragma unroll
;                 for (int bj = 0; bj < 2; ++bj)
; #pragma unroll
;                     for (int n = 0; n < 2; ++n) { const size_t o = r * ldc + col0 + bj * HALF + n * 16; const f32x4 c = *(const f32x4*)(R + o) + acc[ai][bj][m][n];
;                         ss += (c[0] * c[0] + c[1] * c[1]) + (c[2] * c[2] + c[3] * c[3]);
;                         u32x2 w; w.x = cvt_pk_bf16(c[0], c[1]); w.y = cvt_pk_bf16(c[2], c[3]); *(u32x2*)(HB + o) = w; }
.LBB0_3067:
	s_lshl_b32 s41, s48, 8
	s_add_i32 s41, s41, s67
	v_mbcnt_lo_u32_b32 v134, -1, 0
	v_mbcnt_hi_u32_b32 v134, -1, v134
	s_lshl_b32 s48, s12, 2
	s_lshl_b32 s49, s12, 8
	s_or_b32 s49, s49, s70
	s_add_i32 s48, s48, s66
	s_lshl_b32 s48, s48, 2
	v_and_or_b32 v137, v134, 15, s41
	v_lshrrev_b32_e32 v138, 4, v134
	v_lshl_add_u32 v138, v138, 2, s49
	v_lshl_add_u32 v135, v137, 12, v138
	v_lshlrev_b32_e32 v135, 2, v135
	v_lshl_add_u32 v136, v137, 8, s48
	v_cmp_gt_u32_e32 vcc, 16, v134
	v_mov_b32_e32 v250, v135
	global_load_dwordx4 v[146:149], v250, s[36:37] offset:0
	global_load_dwordx4 v[150:153], v250, s[36:37] offset:64
	global_load_dwordx4 v[154:157], v250, s[36:37] offset:512
	global_load_dwordx4 v[158:161], v250, s[36:37] offset:576
	v_add_u32_e32 v251, 0x40000, v135
	global_load_dwordx4 v[162:165], v251, s[36:37] offset:0
	global_load_dwordx4 v[166:169], v251, s[36:37] offset:64
	global_load_dwordx4 v[170:173], v251, s[36:37] offset:512
	global_load_dwordx4 v[174:177], v251, s[36:37] offset:576
	v_add_u32_e32 v252, 0x80000, v135
	global_load_dwordx4 v[178:181], v252, s[36:37] offset:0
	global_load_dwordx4 v[182:185], v252, s[36:37] offset:64
	global_load_dwordx4 v[186:189], v252, s[36:37] offset:512
	global_load_dwordx4 v[190:193], v252, s[36:37] offset:576
	v_add_u32_e32 v250, 0xc0000, v135
	global_load_dwordx4 v[194:197], v250, s[36:37] offset:0
	global_load_dwordx4 v[198:201], v250, s[36:37] offset:64
	global_load_dwordx4 v[202:205], v250, s[36:37] offset:512
	global_load_dwordx4 v[206:209], v250, s[36:37] offset:576
	v_add_u32_e32 v251, 0x200000, v135
	global_load_dwordx4 v[210:213], v251, s[36:37] offset:0
	global_load_dwordx4 v[214:217], v251, s[36:37] offset:64
	global_load_dwordx4 v[218:221], v251, s[36:37] offset:512
	global_load_dwordx4 v[222:225], v251, s[36:37] offset:576
	v_add_u32_e32 v252, 0x240000, v135
	global_load_dwordx4 v[226:229], v252, s[36:37] offset:0
	global_load_dwordx4 v[230:233], v252, s[36:37] offset:64
	global_load_dwordx4 v[234:237], v252, s[36:37] offset:512
	global_load_dwordx4 v[238:241], v252, s[36:37] offset:576
	v_lshrrev_b32_e32 v253, 1, v135
	s_waitcnt vmcnt(23)
	v_pk_add_f32 v[126:127], v[126:127], v[146:147]
	v_pk_add_f32 v[128:129], v[128:129], v[148:149]
	v_mul_f32_e32 v139, v127, v127
	v_mul_f32_e32 v140, v129, v129
	v_fmac_f32_e32 v139, v126, v126
	v_fmac_f32_e32 v140, v128, v128
	v_add_f32_e32 v242, v139, v140
	v_cvt_pk_bf16_f32 v126, v126, v127
	v_cvt_pk_bf16_f32 v127, v128, v129
	global_store_dwordx2 v253, v[126:127], s[14:15] offset:0
	s_waitcnt vmcnt(23)
	v_pk_add_f32 v[122:123], v[122:123], v[150:151]
	v_pk_add_f32 v[124:125], v[124:125], v[152:153]
	v_mul_f32_e32 v139, v123, v123
	v_mul_f32_e32 v140, v125, v125
	v_fmac_f32_e32 v139, v122, v122
	v_fmac_f32_e32 v140, v124, v124
	v_add_f32_e32 v139, v139, v140
	v_add_f32_e32 v242, v242, v139
	v_cvt_pk_bf16_f32 v122, v122, v123
	v_cvt_pk_bf16_f32 v123, v124, v125
	global_store_dwordx2 v253, v[122:123], s[14:15] offset:32
	s_waitcnt vmcnt(23)
	v_pk_add_f32 v[118:119], v[118:119], v[154:155]
	v_pk_add_f32 v[120:121], v[120:121], v[156:157]
	v_mul_f32_e32 v139, v119, v119
	v_mul_f32_e32 v140, v121, v121
	v_fmac_f32_e32 v139, v118, v118
	v_fmac_f32_e32 v140, v120, v120
	v_add_f32_e32 v139, v139, v140
	v_add_f32_e32 v242, v242, v139
	v_cvt_pk_bf16_f32 v118, v118, v119
	v_cvt_pk_bf16_f32 v119, v120, v121
	global_store_dwordx2 v253, v[118:119], s[14:15] offset:256
	s_waitcnt vmcnt(23)
	v_pk_add_f32 v[114:115], v[114:115], v[158:159]
	v_pk_add_f32 v[116:117], v[116:117], v[160:161]
	v_mul_f32_e32 v139, v115, v115
	v_mul_f32_e32 v140, v117, v117
	v_fmac_f32_e32 v139, v114, v114
	v_fmac_f32_e32 v140, v116, v116
	v_add_f32_e32 v139, v139, v140
	v_add_f32_e32 v242, v242, v139
	v_cvt_pk_bf16_f32 v114, v114, v115
	v_cvt_pk_bf16_f32 v115, v116, v117
	global_store_dwordx2 v253, v[114:115], s[14:15] offset:288
	v_add_u32_e32 v250, 0x280000, v135
	global_load_dwordx4 v[146:149], v250, s[36:37] offset:0
	global_load_dwordx4 v[150:153], v250, s[36:37] offset:64
	global_load_dwordx4 v[154:157], v250, s[36:37] offset:512
	global_load_dwordx4 v[158:161], v250, s[36:37] offset:576
	v_add_u32_e32 v253, 0x40000, v135
	v_lshrrev_b32_e32 v253, 1, v253
	s_waitcnt vmcnt(27)
	v_pk_add_f32 v[110:111], v[110:111], v[162:163]
	v_pk_add_f32 v[112:113], v[112:113], v[164:165]
	v_mul_f32_e32 v139, v111, v111
	v_mul_f32_e32 v140, v113, v113
	v_fmac_f32_e32 v139, v110, v110
	v_fmac_f32_e32 v140, v112, v112
	v_add_f32_e32 v243, v139, v140
	v_cvt_pk_bf16_f32 v110, v110, v111
	v_cvt_pk_bf16_f32 v111, v112, v113
	global_store_dwordx2 v253, v[110:111], s[14:15] offset:0
	s_waitcnt vmcnt(27)
	v_pk_add_f32 v[106:107], v[106:107], v[166:167]
	v_pk_add_f32 v[108:109], v[108:109], v[168:169]
	v_mul_f32_e32 v139, v107, v107
	v_mul_f32_e32 v140, v109, v109
	v_fmac_f32_e32 v139, v106, v106
	v_fmac_f32_e32 v140, v108, v108
	v_add_f32_e32 v139, v139, v140
	v_add_f32_e32 v243, v243, v139
	v_cvt_pk_bf16_f32 v106, v106, v107
	v_cvt_pk_bf16_f32 v107, v108, v109
	global_store_dwordx2 v253, v[106:107], s[14:15] offset:32
	s_waitcnt vmcnt(27)
	v_pk_add_f32 v[102:103], v[102:103], v[170:171]
	v_pk_add_f32 v[104:105], v[104:105], v[172:173]
	v_mul_f32_e32 v139, v103, v103
	v_mul_f32_e32 v140, v105, v105
	v_fmac_f32_e32 v139, v102, v102
	v_fmac_f32_e32 v140, v104, v104
	v_add_f32_e32 v139, v139, v140
	v_add_f32_e32 v243, v243, v139
	v_cvt_pk_bf16_f32 v102, v102, v103
	v_cvt_pk_bf16_f32 v103, v104, v105
	global_store_dwordx2 v253, v[102:103], s[14:15] offset:256
	s_waitcnt vmcnt(27)
; __device__ __forceinline__ unsigned cvt_pk_bf16(float lo, float hi) { unsigned r; asm volatile("v_cvt_pk_bf16_f32 %0, %1, %2" : "=v"(r) : "v"(lo), "v"(hi)); return r; }
;     __device__ __forceinline__ void operator()(const f32x4 (&acc)[2][2][4][2], const Unit& u, int wr, int wc, int fr_, int fq_) const {
;     ...
;             for (int m = 0; m < 4; ++m) { const size_t r = (size_t)(row0 + ai * HALF + m * 16); float ss = 0.f;
; #pragma unroll
;                 for (int bj = 0; bj < 2; ++bj)
; #pragma unroll
;                     for (int n = 0; n < 2; ++n) { const size_t o = r * ldc + col0 + bj * HALF + n * 16; const f32x4 c = *(const f32x4*)(R + o) + acc[ai][bj][m][n];
;                         ss += (c[0] * c[0] + c[1] * c[1]) + (c[2] * c[2] + c[3] * c[3]);
;                         u32x2 w; w.x = cvt_pk_bf16(c[0], c[1]); w.y = cvt_pk_bf16(c[2], c[3]); *(u32x2*)(HB + o) = w; }
	v_pk_add_f32 v[98:99], v[98:99], v[174:175]
	v_pk_add_f32 v[100:101], v[100:101], v[176:177]
	v_mul_f32_e32 v139, v99, v99
	v_mul_f32_e32 v140, v101, v101
	v_fmac_f32_e32 v139, v98, v98
	v_fmac_f32_e32 v140, v100, v100
	v_add_f32_e32 v139, v139, v140
	v_add_f32_e32 v243, v243, v139
	v_cvt_pk_bf16_f32 v98, v98, v99
	v_cvt_pk_bf16_f32 v99, v100, v101
	global_store_dwordx2 v253, v[98:99], s[14:15] offset:288
	v_add_u32_e32 v251, 0x2c0000, v135
	global_load_dwordx4 v[162:165], v251, s[36:37] offset:0
	global_load_dwordx4 v[166:169], v251, s[36:37] offset:64
	global_load_dwordx4 v[170:173], v251, s[36:37] offset:512
	global_load_dwordx4 v[174:177], v251, s[36:37] offset:576
	v_add_u32_e32 v253, 0x80000, v135
	v_lshrrev_b32_e32 v253, 1, v253
	s_waitcnt vmcnt(31)
	v_pk_add_f32 v[94:95], v[94:95], v[178:179]
	v_pk_add_f32 v[96:97], v[96:97], v[180:181]
	v_mul_f32_e32 v139, v95, v95
	v_mul_f32_e32 v140, v97, v97
	v_fmac_f32_e32 v139, v94, v94
	v_fmac_f32_e32 v140, v96, v96
	v_add_f32_e32 v244, v139, v140
	v_cvt_pk_bf16_f32 v94, v94, v95
	v_cvt_pk_bf16_f32 v95, v96, v97
	global_store_dwordx2 v253, v[94:95], s[14:15] offset:0
	s_waitcnt vmcnt(31)
	v_pk_add_f32 v[90:91], v[90:91], v[182:183]
	v_pk_add_f32 v[92:93], v[92:93], v[184:185]
	v_mul_f32_e32 v139, v91, v91
	v_mul_f32_e32 v140, v93, v93
	v_fmac_f32_e32 v139, v90, v90
	v_fmac_f32_e32 v140, v92, v92
	v_add_f32_e32 v139, v139, v140
	v_add_f32_e32 v244, v244, v139
	v_cvt_pk_bf16_f32 v90, v90, v91
	v_cvt_pk_bf16_f32 v91, v92, v93
	global_store_dwordx2 v253, v[90:91], s[14:15] offset:32
	s_waitcnt vmcnt(31)
	v_pk_add_f32 v[86:87], v[86:87], v[186:187]
	v_pk_add_f32 v[88:89], v[88:89], v[188:189]
	v_mul_f32_e32 v139, v87, v87
	v_mul_f32_e32 v140, v89, v89
	v_fmac_f32_e32 v139, v86, v86
	v_fmac_f32_e32 v140, v88, v88
	v_add_f32_e32 v139, v139, v140
	v_add_f32_e32 v244, v244, v139
	v_cvt_pk_bf16_f32 v86, v86, v87
	v_cvt_pk_bf16_f32 v87, v88, v89
	global_store_dwordx2 v253, v[86:87], s[14:15] offset:256
	s_waitcnt vmcnt(31)
	v_pk_add_f32 v[82:83], v[82:83], v[190:191]
	v_pk_add_f32 v[84:85], v[84:85], v[192:193]
	v_mul_f32_e32 v139, v83, v83
	v_mul_f32_e32 v140, v85, v85
	v_fmac_f32_e32 v139, v82, v82
	v_fmac_f32_e32 v140, v84, v84
	v_add_f32_e32 v139, v139, v140
	v_add_f32_e32 v244, v244, v139
	v_cvt_pk_bf16_f32 v82, v82, v83
	v_cvt_pk_bf16_f32 v83, v84, v85
	global_store_dwordx2 v253, v[82:83], s[14:15] offset:288
	v_add_u32_e32 v253, 0xc0000, v135
	v_lshrrev_b32_e32 v253, 1, v253
	s_waitcnt vmcnt(31)
	v_pk_add_f32 v[78:79], v[78:79], v[194:195]
	v_pk_add_f32 v[80:81], v[80:81], v[196:197]
	v_mul_f32_e32 v139, v79, v79
	v_mul_f32_e32 v140, v81, v81
	v_fmac_f32_e32 v139, v78, v78
	v_fmac_f32_e32 v140, v80, v80
	v_add_f32_e32 v245, v139, v140
	v_cvt_pk_bf16_f32 v78, v78, v79
	v_cvt_pk_bf16_f32 v79, v80, v81
	global_store_dwordx2 v253, v[78:79], s[14:15] offset:0
	s_waitcnt vmcnt(31)
	v_pk_add_f32 v[74:75], v[74:75], v[198:199]
	v_pk_add_f32 v[76:77], v[76:77], v[200:201]
	v_mul_f32_e32 v139, v75, v75
	v_mul_f32_e32 v140, v77, v77
	v_fmac_f32_e32 v139, v74, v74
	v_fmac_f32_e32 v140, v76, v76
	v_add_f32_e32 v139, v139, v140
	v_add_f32_e32 v245, v245, v139
	v_cvt_pk_bf16_f32 v74, v74, v75
	v_cvt_pk_bf16_f32 v75, v76, v77
	global_store_dwordx2 v253, v[74:75], s[14:15] offset:32
	s_waitcnt vmcnt(31)
	v_pk_add_f32 v[70:71], v[70:71], v[202:203]
	v_pk_add_f32 v[72:73], v[72:73], v[204:205]
	v_mul_f32_e32 v139, v71, v71
	v_mul_f32_e32 v140, v73, v73
	v_fmac_f32_e32 v139, v70, v70
	v_fmac_f32_e32 v140, v72, v72
	v_add_f32_e32 v139, v139, v140
	v_add_f32_e32 v245, v245, v139
	v_cvt_pk_bf16_f32 v70, v70, v71
	v_cvt_pk_bf16_f32 v71, v72, v73
	global_store_dwordx2 v253, v[70:71], s[14:15] offset:256
	s_waitcnt vmcnt(31)
	v_pk_add_f32 v[66:67], v[66:67], v[206:207]
	v_pk_add_f32 v[68:69], v[68:69], v[208:209]
	v_mul_f32_e32 v139, v67, v67
	v_mul_f32_e32 v140, v69, v69
	v_fmac_f32_e32 v139, v66, v66
	v_fmac_f32_e32 v140, v68, v68
	v_add_f32_e32 v139, v139, v140
	v_add_f32_e32 v245, v245, v139
	v_cvt_pk_bf16_f32 v66, v66, v67
	v_cvt_pk_bf16_f32 v67, v68, v69
	global_store_dwordx2 v253, v[66:67], s[14:15] offset:288
	v_add_u32_e32 v253, 0x200000, v135
	v_lshrrev_b32_e32 v253, 1, v253
	s_waitcnt vmcnt(31)
	v_pk_add_f32 v[62:63], v[62:63], v[210:211]
	v_pk_add_f32 v[64:65], v[64:65], v[212:213]
	v_mul_f32_e32 v139, v63, v63
	v_mul_f32_e32 v140, v65, v65
	v_fmac_f32_e32 v139, v62, v62
	v_fmac_f32_e32 v140, v64, v64
	v_add_f32_e32 v246, v139, v140
	v_cvt_pk_bf16_f32 v62, v62, v63
	v_cvt_pk_bf16_f32 v63, v64, v65
	global_store_dwordx2 v253, v[62:63], s[14:15] offset:0
	s_waitcnt vmcnt(31)
	v_pk_add_f32 v[58:59], v[58:59], v[214:215]
	v_pk_add_f32 v[60:61], v[60:61], v[216:217]
	v_mul_f32_e32 v139, v59, v59
	v_mul_f32_e32 v140, v61, v61
	v_fmac_f32_e32 v139, v58, v58
	v_fmac_f32_e32 v140, v60, v60
	v_add_f32_e32 v139, v139, v140
	v_add_f32_e32 v246, v246, v139
	v_cvt_pk_bf16_f32 v58, v58, v59
	v_cvt_pk_bf16_f32 v59, v60, v61
	global_store_dwordx2 v253, v[58:59], s[14:15] offset:32
	s_waitcnt vmcnt(31)
	v_pk_add_f32 v[54:55], v[54:55], v[218:219]
	v_pk_add_f32 v[56:57], v[56:57], v[220:221]
	v_mul_f32_e32 v139, v55, v55
	v_mul_f32_e32 v140, v57, v57
	v_fmac_f32_e32 v139, v54, v54
	v_fmac_f32_e32 v140, v56, v56
	v_add_f32_e32 v139, v139, v140
	v_add_f32_e32 v246, v246, v139
	v_cvt_pk_bf16_f32 v54, v54, v55
	v_cvt_pk_bf16_f32 v55, v56, v57
	global_store_dwordx2 v253, v[54:55], s[14:15] offset:256
	s_waitcnt vmcnt(31)
; __device__ __forceinline__ unsigned cvt_pk_bf16(float lo, float hi) { unsigned r; asm volatile("v_cvt_pk_bf16_f32 %0, %1, %2" : "=v"(r) : "v"(lo), "v"(hi)); return r; }
;     __device__ __forceinline__ void operator()(const f32x4 (&acc)[2][2][4][2], const Unit& u, int wr, int wc, int fr_, int fq_) const {
;     ...
;             for (int m = 0; m < 4; ++m) { const size_t r = (size_t)(row0 + ai * HALF + m * 16); float ss = 0.f;
; #pragma unroll
;                 for (int bj = 0; bj < 2; ++bj)
; #pragma unroll
;                     for (int n = 0; n < 2; ++n) { const size_t o = r * ldc + col0 + bj * HALF + n * 16; const f32x4 c = *(const f32x4*)(R + o) + acc[ai][bj][m][n];
;                         ss += (c[0] * c[0] + c[1] * c[1]) + (c[2] * c[2] + c[3] * c[3]);
;                         u32x2 w; w.x = cvt_pk_bf16(c[0], c[1]); w.y = cvt_pk_bf16(c[2], c[3]); *(u32x2*)(HB + o) = w; }
	v_pk_add_f32 v[50:51], v[50:51], v[222:223]
	v_pk_add_f32 v[52:53], v[52:53], v[224:225]
	v_mul_f32_e32 v139, v51, v51
	v_mul_f32_e32 v140, v53, v53
	v_fmac_f32_e32 v139, v50, v50
	v_fmac_f32_e32 v140, v52, v52
	v_add_f32_e32 v139, v139, v140
	v_add_f32_e32 v246, v246, v139
	v_cvt_pk_bf16_f32 v50, v50, v51
	v_cvt_pk_bf16_f32 v51, v52, v53
	global_store_dwordx2 v253, v[50:51], s[14:15] offset:288
	v_add_u32_e32 v253, 0x240000, v135
	v_lshrrev_b32_e32 v253, 1, v253
	s_waitcnt vmcnt(31)
	v_pk_add_f32 v[46:47], v[46:47], v[226:227]
	v_pk_add_f32 v[48:49], v[48:49], v[228:229]
	v_mul_f32_e32 v139, v47, v47
	v_mul_f32_e32 v140, v49, v49
	v_fmac_f32_e32 v139, v46, v46
	v_fmac_f32_e32 v140, v48, v48
	v_add_f32_e32 v247, v139, v140
	v_cvt_pk_bf16_f32 v46, v46, v47
	v_cvt_pk_bf16_f32 v47, v48, v49
	global_store_dwordx2 v253, v[46:47], s[14:15] offset:0
	s_waitcnt vmcnt(31)
	v_pk_add_f32 v[42:43], v[42:43], v[230:231]
	v_pk_add_f32 v[44:45], v[44:45], v[232:233]
	v_mul_f32_e32 v139, v43, v43
	v_mul_f32_e32 v140, v45, v45
	v_fmac_f32_e32 v139, v42, v42
	v_fmac_f32_e32 v140, v44, v44
	v_add_f32_e32 v139, v139, v140
	v_add_f32_e32 v247, v247, v139
	v_cvt_pk_bf16_f32 v42, v42, v43
	v_cvt_pk_bf16_f32 v43, v44, v45
	global_store_dwordx2 v253, v[42:43], s[14:15] offset:32
	s_waitcnt vmcnt(31)
	v_pk_add_f32 v[38:39], v[38:39], v[234:235]
	v_pk_add_f32 v[40:41], v[40:41], v[236:237]
	v_mul_f32_e32 v139, v39, v39
	v_mul_f32_e32 v140, v41, v41
	v_fmac_f32_e32 v139, v38, v38
	v_fmac_f32_e32 v140, v40, v40
	v_add_f32_e32 v139, v139, v140
	v_add_f32_e32 v247, v247, v139
	v_cvt_pk_bf16_f32 v38, v38, v39
	v_cvt_pk_bf16_f32 v39, v40, v41
	global_store_dwordx2 v253, v[38:39], s[14:15] offset:256
	s_waitcnt vmcnt(31)
	v_pk_add_f32 v[34:35], v[34:35], v[238:239]
	v_pk_add_f32 v[36:37], v[36:37], v[240:241]
	v_mul_f32_e32 v139, v35, v35
	v_mul_f32_e32 v140, v37, v37
	v_fmac_f32_e32 v139, v34, v34
	v_fmac_f32_e32 v140, v36, v36
	v_add_f32_e32 v139, v139, v140
	v_add_f32_e32 v247, v247, v139
	v_cvt_pk_bf16_f32 v34, v34, v35
	v_cvt_pk_bf16_f32 v35, v36, v37
	global_store_dwordx2 v253, v[34:35], s[14:15] offset:288
	v_add_u32_e32 v253, 0x280000, v135
	v_lshrrev_b32_e32 v253, 1, v253
	s_waitcnt vmcnt(27)
	v_pk_add_f32 v[30:31], v[30:31], v[146:147]
	v_pk_add_f32 v[32:33], v[32:33], v[148:149]
	v_mul_f32_e32 v139, v31, v31
	v_mul_f32_e32 v140, v33, v33
	v_fmac_f32_e32 v139, v30, v30
	v_fmac_f32_e32 v140, v32, v32
	v_add_f32_e32 v248, v139, v140
	v_cvt_pk_bf16_f32 v30, v30, v31
	v_cvt_pk_bf16_f32 v31, v32, v33
	global_store_dwordx2 v253, v[30:31], s[14:15] offset:0
	s_waitcnt vmcnt(27)
	v_pk_add_f32 v[26:27], v[26:27], v[150:151]
	v_pk_add_f32 v[28:29], v[28:29], v[152:153]
	v_mul_f32_e32 v139, v27, v27
	v_mul_f32_e32 v140, v29, v29
	v_fmac_f32_e32 v139, v26, v26
	v_fmac_f32_e32 v140, v28, v28
	v_add_f32_e32 v139, v139, v140
	v_add_f32_e32 v248, v248, v139
	v_cvt_pk_bf16_f32 v26, v26, v27
	v_cvt_pk_bf16_f32 v27, v28, v29
	global_store_dwordx2 v253, v[26:27], s[14:15] offset:32
	s_waitcnt vmcnt(27)
	v_pk_add_f32 v[22:23], v[22:23], v[154:155]
	v_pk_add_f32 v[24:25], v[24:25], v[156:157]
	v_mul_f32_e32 v139, v23, v23
	v_mul_f32_e32 v140, v25, v25
	v_fmac_f32_e32 v139, v22, v22
	v_fmac_f32_e32 v140, v24, v24
	v_add_f32_e32 v139, v139, v140
	v_add_f32_e32 v248, v248, v139
	v_cvt_pk_bf16_f32 v22, v22, v23
	v_cvt_pk_bf16_f32 v23, v24, v25
	global_store_dwordx2 v253, v[22:23], s[14:15] offset:256
	s_waitcnt vmcnt(27)
	v_pk_add_f32 v[18:19], v[18:19], v[158:159]
	v_pk_add_f32 v[20:21], v[20:21], v[160:161]
	v_mul_f32_e32 v139, v19, v19
	v_mul_f32_e32 v140, v21, v21
	v_fmac_f32_e32 v139, v18, v18
	v_fmac_f32_e32 v140, v20, v20
	v_add_f32_e32 v139, v139, v140
	v_add_f32_e32 v248, v248, v139
	v_cvt_pk_bf16_f32 v18, v18, v19
	v_cvt_pk_bf16_f32 v19, v20, v21
	global_store_dwordx2 v253, v[18:19], s[14:15] offset:288
	v_add_u32_e32 v253, 0x2c0000, v135
	v_lshrrev_b32_e32 v253, 1, v253
	s_waitcnt vmcnt(23)
; __device__ __forceinline__ unsigned cvt_pk_bf16(float lo, float hi) { unsigned r; asm volatile("v_cvt_pk_bf16_f32 %0, %1, %2" : "=v"(r) : "v"(lo), "v"(hi)); return r; }
;     __device__ __forceinline__ void operator()(const f32x4 (&acc)[2][2][4][2], const Unit& u, int wr, int wc, int fr_, int fq_) const {
;     ...
;                     for (int n = 0; n < 2; ++n) { const size_t o = r * ldc + col0 + bj * HALF + n * 16; const f32x4 c = *(const f32x4*)(R + o) + acc[ai][bj][m][n];
;                         ss += (c[0] * c[0] + c[1] * c[1]) + (c[2] * c[2] + c[3] * c[3]);
;                         u32x2 w; w.x = cvt_pk_bf16(c[0], c[1]); w.y = cvt_pk_bf16(c[2], c[3]); *(u32x2*)(HB + o) = w; }
;                 ss += __builtin_bit_cast(float, __builtin_amdgcn_ds_bpermute((l_ ^ 16) << 2, __builtin_bit_cast(int, ss)));
;                 ss += __builtin_bit_cast(float, __builtin_amdgcn_ds_bpermute((l_ ^ 32) << 2, __builtin_bit_cast(int, ss)));
;                 if (fq == 0) PSQ[r * 64 + u.pn * 4 + wc] = ss;
	v_pk_add_f32 v[14:15], v[14:15], v[162:163]
	v_pk_add_f32 v[16:17], v[16:17], v[164:165]
	v_mul_f32_e32 v139, v15, v15
	v_mul_f32_e32 v140, v17, v17
	v_fmac_f32_e32 v139, v14, v14
	v_fmac_f32_e32 v140, v16, v16
	v_add_f32_e32 v249, v139, v140
	v_cvt_pk_bf16_f32 v14, v14, v15
	v_cvt_pk_bf16_f32 v15, v16, v17
	global_store_dwordx2 v253, v[14:15], s[14:15] offset:0
	s_waitcnt vmcnt(23)
	v_pk_add_f32 v[10:11], v[10:11], v[166:167]
	v_pk_add_f32 v[12:13], v[12:13], v[168:169]
	v_mul_f32_e32 v139, v11, v11
	v_mul_f32_e32 v140, v13, v13
	v_fmac_f32_e32 v139, v10, v10
	v_fmac_f32_e32 v140, v12, v12
	v_add_f32_e32 v139, v139, v140
	v_add_f32_e32 v249, v249, v139
	v_cvt_pk_bf16_f32 v10, v10, v11
	v_cvt_pk_bf16_f32 v11, v12, v13
	global_store_dwordx2 v253, v[10:11], s[14:15] offset:32
	s_waitcnt vmcnt(23)
	v_pk_add_f32 v[6:7], v[6:7], v[170:171]
	v_pk_add_f32 v[8:9], v[8:9], v[172:173]
	v_mul_f32_e32 v139, v7, v7
	v_mul_f32_e32 v140, v9, v9
	v_fmac_f32_e32 v139, v6, v6
	v_fmac_f32_e32 v140, v8, v8
	v_add_f32_e32 v139, v139, v140
	v_add_f32_e32 v249, v249, v139
	v_cvt_pk_bf16_f32 v6, v6, v7
	v_cvt_pk_bf16_f32 v7, v8, v9
	global_store_dwordx2 v253, v[6:7], s[14:15] offset:256
	s_waitcnt vmcnt(23)
	v_pk_add_f32 v[2:3], v[2:3], v[174:175]
	v_pk_add_f32 v[4:5], v[4:5], v[176:177]
	v_mul_f32_e32 v139, v3, v3
	v_mul_f32_e32 v140, v5, v5
	v_fmac_f32_e32 v139, v2, v2
	v_fmac_f32_e32 v140, v4, v4
	v_add_f32_e32 v139, v139, v140
	v_add_f32_e32 v249, v249, v139
	v_cvt_pk_bf16_f32 v2, v2, v3
	v_cvt_pk_bf16_f32 v3, v4, v5
	global_store_dwordx2 v253, v[2:3], s[14:15] offset:288
	v_lshlrev_b32_e32 v137, 2, v134
	v_xor_b32_e32 v138, 64, v137
	v_xor_b32_e32 v137, 0x80, v137
	ds_bpermute_b32 v114, v138, v242
	ds_bpermute_b32 v115, v138, v243
	ds_bpermute_b32 v116, v138, v244
	ds_bpermute_b32 v117, v138, v245
	ds_bpermute_b32 v118, v138, v246
	ds_bpermute_b32 v119, v138, v247
	ds_bpermute_b32 v120, v138, v248
	ds_bpermute_b32 v121, v138, v249
	s_waitcnt lgkmcnt(0)
	v_add_f32_e32 v242, v242, v114
	v_add_f32_e32 v243, v243, v115
	v_add_f32_e32 v244, v244, v116
	v_add_f32_e32 v245, v245, v117
	v_add_f32_e32 v246, v246, v118
	v_add_f32_e32 v247, v247, v119
	v_add_f32_e32 v248, v248, v120
	v_add_f32_e32 v249, v249, v121
	ds_bpermute_b32 v114, v137, v242
	ds_bpermute_b32 v115, v137, v243
	ds_bpermute_b32 v116, v137, v244
	ds_bpermute_b32 v117, v137, v245
	ds_bpermute_b32 v118, v137, v246
	ds_bpermute_b32 v119, v137, v247
	ds_bpermute_b32 v120, v137, v248
	ds_bpermute_b32 v121, v137, v249
	s_waitcnt lgkmcnt(0)
	v_add_f32_e32 v242, v242, v114
	v_add_f32_e32 v243, v243, v115
	v_add_f32_e32 v244, v244, v116
	v_add_f32_e32 v245, v245, v117
	v_add_f32_e32 v246, v246, v118
	v_add_f32_e32 v247, v247, v119
	v_add_f32_e32 v248, v248, v120
	v_add_f32_e32 v249, v249, v121
	s_and_saveexec_b64 s[50:51], vcc
	global_store_dword v136, v242, s[16:17]
	v_add_u32_e32 v99, 0x1000, v136
	global_store_dword v99, v243, s[16:17]
	v_add_u32_e32 v100, 0x2000, v136
	global_store_dword v100, v244, s[16:17]
	v_add_u32_e32 v101, 0x3000, v136
	global_store_dword v101, v245, s[16:17]
	v_add_u32_e32 v102, 0x8000, v136
	global_store_dword v102, v246, s[16:17]
	v_add_u32_e32 v103, 0x9000, v136
	global_store_dword v103, v247, s[16:17]
	v_add_u32_e32 v104, 0xa000, v136
	global_store_dword v104, v248, s[16:17]
	v_add_u32_e32 v105, 0xb000, v136
	global_store_dword v105, v249, s[16:17]
	s_or_b64 exec, exec, s[50:51]
	s_andn2_b64 vcc, exec, s[0:1]
	s_mov_b64 s[0:1], -1
	s_cbranch_vccnz .LBB0_3056
	s_andn2_b64 vcc, exec, s[10:11]
	s_cbranch_vccnz .LBB0_3055
	s_barrier
	s_branch .LBB0_3055
